# mixout MFMA mat-vec: rolling ds_read prefetch of the B fragments inside the MFMA shadow (counted lgkmcnt waits)
# baseline (speedup 1.0000x reference)
.LBB0_1234:
	v_and_b32_e32 v230, 15, v203
	v_lshrrev_b32_e32 v224, 4, v203
	v_lshlrev_b32_e32 v2, 8, v230
	v_lshl_add_u32 v2, v224, 6, v2
	ds_read_b128 v[194:197], v2
	ds_read_b128 v[204:207], v2 offset:16
	ds_read_b128 v[226:229], v2 offset:32
	ds_read_b128 v[68:71], v2 offset:48
	v_readfirstlane_b32 s0, v0
	v_lshlrev_b32_e32 v3, 14, v224
	s_lshr_b32 s0, s0, 6
	s_lshl_b32 s0, s0, 7
	v_lshl_add_u32 v230, v230, 3, v3
	v_add_u32_e32 v230, s0, v230
	v_add_u32_e32 v230, 0x2000, v230
	ds_read_b64 v[54:55], v230 offset:0
	ds_read_b64 v[60:61], v230 offset:1024
	ds_read_b64 v[198:199], v230 offset:2048
	ds_read_b64 v[208:209], v230 offset:3072
	s_waitcnt lgkmcnt(3)
	v_mfma_f32_16x16x4_f32 v[64:67], v194, v54, 0
	v_mfma_f32_16x16x4_f32 v[2:5], v194, v55, 0
	s_waitcnt lgkmcnt(2)
	v_mfma_f32_16x16x4_f32 v[64:67], v195, v60, v[64:67]
	v_mfma_f32_16x16x4_f32 v[2:5], v195, v61, v[2:5]
	ds_read_b64 v[54:55], v230 offset:4096
	s_waitcnt lgkmcnt(2)
	v_mfma_f32_16x16x4_f32 v[64:67], v196, v198, v[64:67]
	v_mfma_f32_16x16x4_f32 v[2:5], v196, v199, v[2:5]
	ds_read_b64 v[60:61], v230 offset:5120
	s_waitcnt lgkmcnt(2)
	v_mfma_f32_16x16x4_f32 v[64:67], v197, v208, v[64:67]
	v_mfma_f32_16x16x4_f32 v[2:5], v197, v209, v[2:5]
	ds_read_b64 v[198:199], v230 offset:6144
	s_waitcnt lgkmcnt(2)
	v_mfma_f32_16x16x4_f32 v[64:67], v204, v54, v[64:67]
	v_mfma_f32_16x16x4_f32 v[2:5], v204, v55, v[2:5]
	ds_read_b64 v[208:209], v230 offset:7168
	s_waitcnt lgkmcnt(2)
	v_mfma_f32_16x16x4_f32 v[64:67], v205, v60, v[64:67]
	v_mfma_f32_16x16x4_f32 v[2:5], v205, v61, v[2:5]
	ds_read_b64 v[54:55], v230 offset:8192
	s_waitcnt lgkmcnt(2)
	v_mfma_f32_16x16x4_f32 v[64:67], v206, v198, v[64:67]
	v_mfma_f32_16x16x4_f32 v[2:5], v206, v199, v[2:5]
	ds_read_b64 v[60:61], v230 offset:9216
	s_waitcnt lgkmcnt(2)
	v_mfma_f32_16x16x4_f32 v[64:67], v207, v208, v[64:67]
	v_mfma_f32_16x16x4_f32 v[2:5], v207, v209, v[2:5]
	ds_read_b64 v[198:199], v230 offset:10240
	s_waitcnt lgkmcnt(2)
	v_mfma_f32_16x16x4_f32 v[64:67], v226, v54, v[64:67]
	v_mfma_f32_16x16x4_f32 v[2:5], v226, v55, v[2:5]
	ds_read_b64 v[208:209], v230 offset:11264
	s_waitcnt lgkmcnt(2)
	v_mfma_f32_16x16x4_f32 v[64:67], v227, v60, v[64:67]
	v_mfma_f32_16x16x4_f32 v[2:5], v227, v61, v[2:5]
	ds_read_b64 v[54:55], v230 offset:12288
	s_waitcnt lgkmcnt(2)
	v_mfma_f32_16x16x4_f32 v[64:67], v228, v198, v[64:67]
	v_mfma_f32_16x16x4_f32 v[2:5], v228, v199, v[2:5]
	ds_read_b64 v[60:61], v230 offset:13312
	s_waitcnt lgkmcnt(2)
	v_mfma_f32_16x16x4_f32 v[64:67], v229, v208, v[64:67]
	v_mfma_f32_16x16x4_f32 v[2:5], v229, v209, v[2:5]
	ds_read_b64 v[198:199], v230 offset:14336
	s_waitcnt lgkmcnt(2)
	v_mfma_f32_16x16x4_f32 v[64:67], v68, v54, v[64:67]
	v_mfma_f32_16x16x4_f32 v[2:5], v68, v55, v[2:5]
	ds_read_b64 v[208:209], v230 offset:15360
	s_waitcnt lgkmcnt(2)
	v_mfma_f32_16x16x4_f32 v[64:67], v69, v60, v[64:67]
	v_mfma_f32_16x16x4_f32 v[2:5], v69, v61, v[2:5]
	s_waitcnt lgkmcnt(1)
	v_mfma_f32_16x16x4_f32 v[64:67], v70, v198, v[64:67]
	v_mfma_f32_16x16x4_f32 v[2:5], v70, v199, v[2:5]
	s_waitcnt lgkmcnt(0)
	v_mfma_f32_16x16x4_f32 v[64:67], v71, v208, v[64:67]
	v_mfma_f32_16x16x4_f32 v[2:5], v71, v209, v[2:5]
	s_nop 7
	v_and_b32_e32 v230, 15, v203
	v_lshrrev_b32_e32 v224, 4, v203
	v_lshlrev_b32_e32 v224, 4, v224
	v_lshl_add_u32 v224, v230, 7, v224
	s_lshl_b32 s0, s0, 4
	v_add_u32_e32 v224, s0, v224
	v_add_u32_e32 v224, 0x14000, v224
	s_nop 15
	s_nop 15
	ds_write_b128 v224, v[64:67]
	ds_write_b128 v224, v[2:5] offset:64
	v_and_b32_e32 v230, 0xff, v0
	v_lshrrev_b32_e32 v198, 8, v0
	v_lshlrev_b32_e32 v230, 6, v230
	v_lshl_add_u32 v230, v198, 5, v230
	v_add_u32_e32 v230, 0x14000, v230
	s_waitcnt lgkmcnt(0)
	s_barrier
	ds_read_b64 v[66:67], v230
	ds_read_b64 v[64:65], v230 offset:8
	ds_read_b64 v[60:61], v230 offset:16
	ds_read_b64 v[54:55], v230 offset:24
	s_movk_i32 s0, 0x100
	s_waitcnt lgkmcnt(0)
	v_lshlrev_b32_e32 v196, 16, v170
	v_lshlrev_b32_e32 v237, 16, v172
	v_lshlrev_b32_e32 v236, 16, v173
	v_lshlrev_b32_e32 v233, 16, v176
	global_load_dword v176, v[20:21], off
	global_load_dword v173, v[22:23], off
	global_load_dword v170, v[24:25], off
	global_load_dword v172, v[26:27], off
	v_and_b32_e32 v2, 64, v203
	v_add_u32_e32 v69, 64, v2
	v_xor_b32_e32 v2, 1, v203
	v_cmp_lt_i32_e64 s[2:3], v2, v69
	v_xor_b32_e32 v3, 2, v203
	v_xor_b32_e32 v4, 4, v203
	v_cndmask_b32_e64 v2, v203, v2, s[2:3]
	v_cmp_lt_i32_e64 s[2:3], v3, v69
	v_xor_b32_e32 v5, 8, v203
	v_xor_b32_e32 v68, 16, v203
	v_cndmask_b32_e64 v3, v203, v3, s[2:3]
	v_cmp_lt_i32_e64 s[2:3], v4, v69
	v_lshlrev_b32_e32 v194, 16, v163
	v_lshlrev_b32_e32 v224, 16, v191
	v_cndmask_b32_e64 v4, v203, v4, s[2:3]
	v_cmp_lt_i32_e64 s[2:3], v5, v69
	v_lshlrev_b32_e32 v191, 16, v192
	v_xor_b32_e32 v192, 32, v203
	v_cndmask_b32_e64 v5, v203, v5, s[2:3]
	v_cmp_lt_i32_e64 s[2:3], v68, v69
	v_lshlrev_b32_e32 v183, 16, v183
	v_add_f32_e32 v183, v183, v194
	v_cndmask_b32_e64 v68, v203, v68, s[2:3]
	v_cmp_lt_i32_e64 s[2:3], v192, v69
	v_lshlrev_b32_e32 v2, 2, v2
	v_lshlrev_b32_e32 v3, 2, v3
	v_cndmask_b32_e64 v69, v203, v192, s[2:3]
	v_mul_f32_e32 v192, v183, v183
	s_nop 1
	v_mov_b32_dpp v192, v192 quad_perm:[1,0,3,2] row_mask:0xf bank_mask:0xf
	v_lshlrev_b32_e32 v225, 16, v190
	v_lshlrev_b32_e32 v190, 16, v193
	v_lshlrev_b32_e32 v4, 2, v4
	v_lshlrev_b32_e32 v5, 2, v5
	s_waitcnt lgkmcnt(0)
	v_fmac_f32_e32 v192, v183, v183
	s_nop 1
	v_lshlrev_b32_e32 v68, 2, v68
	v_lshlrev_b32_e32 v69, 2, v69
	v_lshlrev_b32_e32 v184, 16, v184
	v_lshlrev_b32_e32 v195, 16, v169
	s_waitcnt lgkmcnt(0)
	v_add_f32_dpp v192, v192, v192 quad_perm:[2,3,0,1] row_mask:0xf bank_mask:0xf
	s_nop 1
	v_lshlrev_b32_e32 v181, 16, v181
	v_add_f32_e32 v181, v181, v195
	v_lshlrev_b32_e32 v179, 16, v179
	v_mul_f32_e32 v179, v196, v179
	s_waitcnt lgkmcnt(0)
	v_add_f32_dpp v192, v192, v192 row_half_mirror row_mask:0xf bank_mask:0xf
	s_nop 1
	v_lshlrev_b32_e32 v238, 16, v171
	v_lshlrev_b64 v[62:63], 11, v[62:63]
	v_lshl_add_u64 v[62:63], v[28:29], 0, v[62:63]
	v_lshlrev_b32_e32 v235, 16, v174
	s_waitcnt lgkmcnt(0)
	v_add_f32_dpp v192, v192, v192 row_mirror row_mask:0xf bank_mask:0xf
	v_mov_b32_e32 v193, v192
	s_nop 1
	v_permlane16_swap_b32_e32 v193, v192
	v_lshlrev_b32_e32 v234, 16, v175
	v_lshlrev_b64 v[58:59], 11, v[58:59]
	v_lshl_add_u64 v[58:59], v[28:29], 0, v[58:59]
	v_lshlrev_b32_e32 v232, 16, v180
	s_waitcnt lgkmcnt(0)
	v_add_f32_e32 v192, v192, v193
	v_mov_b32_e32 v193, v192
	s_nop 1
	v_permlane32_swap_b32_e32 v193, v192
	v_lshlrev_b32_e32 v231, 16, v182
	v_lshlrev_b32_e32 v230, 16, v185
	v_lshlrev_b64 v[56:57], 11, v[56:57]
	v_lshl_add_u64 v[56:57], v[28:29], 0, v[56:57]
	s_waitcnt lgkmcnt(0)
	v_add_f32_e32 v192, v192, v193
	v_fmamk_f32 v192, v192, 0x3c800000, v165
	v_rsq_f32_e32 v192, v192
	v_lshlrev_b32_e32 v229, 16, v186
	v_lshlrev_b32_e32 v228, 16, v187
	v_lshlrev_b32_e32 v227, 16, v188
	v_mul_f32_e32 v183, v183, v192
	v_mul_f32_e32 v192, 0xbfb8aa3b, v184
	v_exp_f32_e32 v192, v192
	v_lshlrev_b32_e32 v226, 16, v189
	v_lshlrev_b64 v[52:53], 11, v[52:53]
	v_lshl_add_u64 v[52:53], v[28:29], 0, v[52:53]
	v_add_f32_e32 v192, 1.0, v192
	v_rcp_f32_e32 v192, v192
	s_waitcnt vmcnt(3)
	v_mul_f32_e32 v183, v176, v183
	v_lshlrev_b64 v[50:51], 11, v[50:51]
	v_lshl_add_u64 v[50:51], v[28:29], 0, v[50:51]
	v_mul_f32_e32 v184, v192, v184
	v_mul_f32_e32 v183, v184, v183
	s_nop 1
	v_lshlrev_b32_e32 v189, 16, v210
	v_lshlrev_b32_e32 v188, 16, v211
	v_lshlrev_b32_e32 v187, 16, v212
	v_lshlrev_b32_e32 v186, 16, v213
	s_waitcnt lgkmcnt(0)
	v_add_f32_dpp v184, v181, v181 quad_perm:[1,0,3,2] row_mask:0xf bank_mask:0xf
	s_nop 1
	v_lshlrev_b64 v[48:49], 11, v[48:49]
	v_lshl_add_u64 v[48:49], v[28:29], 0, v[48:49]
	v_lshlrev_b32_e32 v185, 16, v214
	v_lshlrev_b32_e32 v182, 16, v215
	s_waitcnt lgkmcnt(0)
	v_add_f32_dpp v184, v184, v184 quad_perm:[2,3,0,1] row_mask:0xf bank_mask:0xf
	s_nop 1
	v_lshlrev_b32_e32 v180, 16, v216
	v_lshlrev_b32_e32 v175, 16, v217
	v_lshlrev_b64 v[46:47], 11, v[46:47]
	v_lshl_add_u64 v[46:47], v[28:29], 0, v[46:47]
	s_waitcnt lgkmcnt(0)
	v_add_f32_dpp v184, v184, v184 row_half_mirror row_mask:0xf bank_mask:0xf
	s_nop 1
	v_lshlrev_b32_e32 v174, 16, v218
	v_lshlrev_b32_e32 v171, 16, v219
	v_lshlrev_b32_e32 v169, 16, v220
	v_lshlrev_b32_e32 v163, 16, v221
	s_waitcnt lgkmcnt(0)
	v_add_f32_dpp v184, v184, v184 row_mirror row_mask:0xf bank_mask:0xf
	v_mov_b32_e32 v192, v184
	s_nop 1
	v_permlane16_swap_b32_e32 v192, v184
	v_lshlrev_b64 v[44:45], 11, v[44:45]
	v_lshl_add_u64 v[44:45], v[28:29], 0, v[44:45]
	v_lshlrev_b32_e32 v71, 16, v222
	v_lshlrev_b32_e32 v70, 16, v223
	s_waitcnt lgkmcnt(0)
	v_add_f32_e32 v184, v184, v192
	v_mov_b32_e32 v192, v184
	s_nop 1
	v_permlane32_swap_b32_e32 v192, v184
	s_waitcnt lgkmcnt(0)
	v_add_f32_e32 v184, v184, v192
	v_fmac_f32_e32 v181, 0xbc800000, v184
	v_mul_f32_e32 v184, v181, v181
	s_nop 1
	v_mov_b32_dpp v184, v184 quad_perm:[1,0,3,2] row_mask:0xf bank_mask:0xf
	s_waitcnt lgkmcnt(0)
	v_fmac_f32_e32 v184, v181, v181
	s_nop 1
	s_waitcnt lgkmcnt(0)
	v_add_f32_dpp v184, v184, v184 quad_perm:[2,3,0,1] row_mask:0xf bank_mask:0xf
	s_nop 1
	s_waitcnt lgkmcnt(0)
	v_add_f32_dpp v184, v184, v184 row_half_mirror row_mask:0xf bank_mask:0xf
	s_nop 1
	s_waitcnt lgkmcnt(0)
	v_add_f32_dpp v184, v184, v184 row_mirror row_mask:0xf bank_mask:0xf
	v_mov_b32_e32 v192, v184
	s_nop 1
	v_permlane16_swap_b32_e32 v192, v184
	s_waitcnt lgkmcnt(0)
	v_add_f32_e32 v184, v184, v192
	v_mov_b32_e32 v192, v184
	s_nop 1
	v_permlane32_swap_b32_e32 v192, v184
	s_waitcnt lgkmcnt(0)
	v_add_f32_e32 v184, v184, v192
	v_fmamk_f32 v184, v184, 0x3c800000, v164
	v_rsq_f32_e32 v184, v184
	s_nop 0
	v_mul_f32_e32 v181, v181, v184
	s_waitcnt vmcnt(0)
	v_mul_f32_e32 v184, v179, v172
	s_nop 1
	v_mov_b32_dpp v184, v184 quad_perm:[1,0,3,2] row_mask:0xf bank_mask:0xf
	v_fma_f32 v181, v173, v181, v170
	s_waitcnt lgkmcnt(0)
	v_fmac_f32_e32 v184, v179, v172
	s_nop 1
	s_waitcnt lgkmcnt(0)
	v_add_f32_dpp v179, v184, v184 quad_perm:[2,3,0,1] row_mask:0xf bank_mask:0xf
	s_nop 1
	s_waitcnt lgkmcnt(0)
	v_add_f32_dpp v179, v179, v179 row_half_mirror row_mask:0xf bank_mask:0xf
	s_nop 1
	s_waitcnt lgkmcnt(0)
	v_add_f32_dpp v179, v179, v179 row_mirror row_mask:0xf bank_mask:0xf
	v_mov_b32_e32 v184, v179
	s_nop 1
	v_permlane16_swap_b32_e32 v184, v179
	s_waitcnt lgkmcnt(0)
	v_add_f32_e32 v179, v179, v184
	v_mov_b32_e32 v184, v179
	s_nop 1
	v_permlane32_swap_b32_e32 v184, v179
	s_waitcnt lgkmcnt(0)
	v_add_f32_e32 v179, v179, v184
	v_fmac_f32_e32 v181, v179, v238
	v_mul_f32_e32 v66, v66, v181
	v_cvt_pk_bf16_f32 v179, v183, s0
	v_cvt_pk_bf16_f32 v66, v66, s0
	global_store_short v[62:63], v179, off
	global_store_short v[62:63], v66, off offset:512
	v_lshlrev_b32_e32 v62, 16, v177
	v_add_f32_e32 v62, v62, v237
	v_mul_f32_e32 v63, v62, v62
	s_nop 1
	v_mov_b32_dpp v63, v63 quad_perm:[1,0,3,2] row_mask:0xf bank_mask:0xf
	s_waitcnt lgkmcnt(0)
	v_fmac_f32_e32 v63, v62, v62
	s_nop 1
	s_waitcnt lgkmcnt(0)
	v_add_f32_dpp v63, v63, v63 quad_perm:[2,3,0,1] row_mask:0xf bank_mask:0xf
	s_nop 1
	s_waitcnt lgkmcnt(0)
	v_add_f32_dpp v63, v63, v63 row_half_mirror row_mask:0xf bank_mask:0xf
	s_nop 1
	s_waitcnt lgkmcnt(0)
	v_add_f32_dpp v63, v63, v63 row_mirror row_mask:0xf bank_mask:0xf
	v_mov_b32_e32 v66, v63
	s_nop 1
	v_permlane16_swap_b32_e32 v66, v63
	s_waitcnt lgkmcnt(0)
	v_add_f32_e32 v63, v63, v66
	v_mov_b32_e32 v66, v63
	s_nop 1
	v_permlane32_swap_b32_e32 v66, v63
	s_waitcnt lgkmcnt(0)
	v_add_f32_e32 v63, v63, v66
	v_fmamk_f32 v63, v63, 0x3c800000, v165
	v_rsq_f32_e32 v63, v63
	s_nop 0
	v_mul_f32_e32 v62, v62, v63
	v_lshlrev_b32_e32 v63, 16, v178
	v_mul_f32_e32 v66, 0xbfb8aa3b, v63
	v_exp_f32_e32 v66, v66
	v_mul_f32_e32 v62, v176, v62
	v_add_f32_e32 v66, 1.0, v66
	v_rcp_f32_e32 v66, v66
	s_nop 0
	v_mul_f32_e32 v63, v66, v63
	v_mul_f32_e32 v62, v63, v62
	v_lshlrev_b32_e32 v63, 16, v162
	v_add_f32_e32 v63, v63, v236
	s_nop 1
	v_cvt_pk_bf16_f32 v62, v62, s0
	global_store_short v[58:59], v62, off
	s_waitcnt lgkmcnt(0)
	v_add_f32_dpp v66, v63, v63 quad_perm:[1,0,3,2] row_mask:0xf bank_mask:0xf
	s_nop 1
	s_waitcnt lgkmcnt(0)
	v_add_f32_dpp v66, v66, v66 quad_perm:[2,3,0,1] row_mask:0xf bank_mask:0xf
	s_nop 1
	s_waitcnt lgkmcnt(0)
	v_add_f32_dpp v66, v66, v66 row_half_mirror row_mask:0xf bank_mask:0xf
	s_nop 1
	s_waitcnt lgkmcnt(0)
	v_add_f32_dpp v66, v66, v66 row_mirror row_mask:0xf bank_mask:0xf
	v_mov_b32_e32 v162, v66
	s_nop 1
	v_permlane16_swap_b32_e32 v162, v66
	s_waitcnt lgkmcnt(0)
	v_add_f32_e32 v66, v66, v162
	v_mov_b32_e32 v162, v66
	s_nop 1
	v_permlane32_swap_b32_e32 v162, v66
	s_waitcnt lgkmcnt(0)
	v_add_f32_e32 v66, v66, v162
	v_fmac_f32_e32 v63, 0xbc800000, v66
	v_mul_f32_e32 v66, v63, v63
	s_nop 1
	v_mov_b32_dpp v66, v66 quad_perm:[1,0,3,2] row_mask:0xf bank_mask:0xf
	s_waitcnt lgkmcnt(0)
	v_fmac_f32_e32 v66, v63, v63
	s_nop 1
	s_waitcnt lgkmcnt(0)
	v_add_f32_dpp v66, v66, v66 quad_perm:[2,3,0,1] row_mask:0xf bank_mask:0xf
	s_nop 1
	s_waitcnt lgkmcnt(0)
	v_add_f32_dpp v66, v66, v66 row_half_mirror row_mask:0xf bank_mask:0xf
	s_nop 1
	s_waitcnt lgkmcnt(0)
	v_add_f32_dpp v66, v66, v66 row_mirror row_mask:0xf bank_mask:0xf
	v_mov_b32_e32 v162, v66
	s_nop 1
	v_permlane16_swap_b32_e32 v162, v66
	s_waitcnt lgkmcnt(0)
	v_add_f32_e32 v66, v66, v162
	v_mov_b32_e32 v162, v66
	s_nop 1
	v_permlane32_swap_b32_e32 v162, v66
	s_waitcnt lgkmcnt(0)
	v_add_f32_e32 v66, v66, v162
	v_fmamk_f32 v66, v66, 0x3c800000, v164
	v_rsq_f32_e32 v66, v66
	s_nop 0
	v_mul_f32_e32 v63, v63, v66
	v_lshlrev_b32_e32 v66, 16, v161
	v_mul_f32_e32 v66, v235, v66
	v_mul_f32_e32 v161, v66, v172
	s_nop 1
	v_mov_b32_dpp v161, v161 quad_perm:[1,0,3,2] row_mask:0xf bank_mask:0xf
	v_fma_f32 v63, v173, v63, v170
	s_waitcnt lgkmcnt(0)
	v_fmac_f32_e32 v161, v66, v172
	s_nop 1
	s_waitcnt lgkmcnt(0)
	v_add_f32_dpp v66, v161, v161 quad_perm:[2,3,0,1] row_mask:0xf bank_mask:0xf
	s_nop 1
	s_waitcnt lgkmcnt(0)
	v_add_f32_dpp v66, v66, v66 row_half_mirror row_mask:0xf bank_mask:0xf
	s_nop 1
	s_waitcnt lgkmcnt(0)
	v_add_f32_dpp v66, v66, v66 row_mirror row_mask:0xf bank_mask:0xf
	v_mov_b32_e32 v161, v66
	s_nop 1
	v_permlane16_swap_b32_e32 v161, v66
	s_waitcnt lgkmcnt(0)
	v_add_f32_e32 v66, v66, v161
	v_mov_b32_e32 v161, v66
	s_nop 1
	v_permlane32_swap_b32_e32 v161, v66
	s_waitcnt lgkmcnt(0)
	v_add_f32_e32 v66, v66, v161
	v_fmac_f32_e32 v63, v66, v234
	v_mul_f32_e32 v63, v67, v63
	v_cvt_pk_bf16_f32 v62, v63, s0
	global_store_short v[58:59], v62, off offset:512
	v_lshlrev_b32_e32 v58, 16, v159
	v_add_f32_e32 v58, v58, v233
	v_mul_f32_e32 v59, v58, v58
	s_nop 1
	v_mov_b32_dpp v59, v59 quad_perm:[1,0,3,2] row_mask:0xf bank_mask:0xf
	s_waitcnt lgkmcnt(0)
	v_fmac_f32_e32 v59, v58, v58
	s_nop 1
	s_waitcnt lgkmcnt(0)
	v_add_f32_dpp v59, v59, v59 quad_perm:[2,3,0,1] row_mask:0xf bank_mask:0xf
	s_nop 1
	s_waitcnt lgkmcnt(0)
	v_add_f32_dpp v59, v59, v59 row_half_mirror row_mask:0xf bank_mask:0xf
	s_nop 1
	s_waitcnt lgkmcnt(0)
	v_add_f32_dpp v59, v59, v59 row_mirror row_mask:0xf bank_mask:0xf
	v_mov_b32_e32 v62, v59
	s_nop 1
	v_permlane16_swap_b32_e32 v62, v59
	s_waitcnt lgkmcnt(0)
	v_add_f32_e32 v59, v59, v62
	v_mov_b32_e32 v62, v59
	s_nop 1
	v_permlane32_swap_b32_e32 v62, v59
	s_waitcnt lgkmcnt(0)
	v_add_f32_e32 v59, v59, v62
	v_fmamk_f32 v59, v59, 0x3c800000, v165
	v_rsq_f32_e32 v59, v59
	s_nop 0
	v_mul_f32_e32 v58, v58, v59
	v_lshlrev_b32_e32 v59, 16, v160
	v_mul_f32_e32 v62, 0xbfb8aa3b, v59
	v_exp_f32_e32 v62, v62
	v_mul_f32_e32 v58, v176, v58
	v_add_f32_e32 v62, 1.0, v62
	v_rcp_f32_e32 v62, v62
	s_nop 0
	v_mul_f32_e32 v59, v62, v59
	v_mul_f32_e32 v58, v59, v58
	v_lshlrev_b32_e32 v59, 16, v158
	v_add_f32_e32 v59, v59, v232
	s_nop 1
	v_cvt_pk_bf16_f32 v58, v58, s0
	global_store_short v[56:57], v58, off
	s_waitcnt lgkmcnt(0)
	v_add_f32_dpp v62, v59, v59 quad_perm:[1,0,3,2] row_mask:0xf bank_mask:0xf
	s_nop 1
	s_waitcnt lgkmcnt(0)
	v_add_f32_dpp v62, v62, v62 quad_perm:[2,3,0,1] row_mask:0xf bank_mask:0xf
	s_nop 1
	s_waitcnt lgkmcnt(0)
	v_add_f32_dpp v62, v62, v62 row_half_mirror row_mask:0xf bank_mask:0xf
	s_nop 1
	s_waitcnt lgkmcnt(0)
	v_add_f32_dpp v62, v62, v62 row_mirror row_mask:0xf bank_mask:0xf
	v_mov_b32_e32 v63, v62
	s_nop 1
	v_permlane16_swap_b32_e32 v63, v62
	s_waitcnt lgkmcnt(0)
	v_add_f32_e32 v62, v62, v63
	v_mov_b32_e32 v63, v62
	s_nop 1
	v_permlane32_swap_b32_e32 v63, v62
	s_waitcnt lgkmcnt(0)
	v_add_f32_e32 v62, v62, v63
	v_fmac_f32_e32 v59, 0xbc800000, v62
	v_mul_f32_e32 v62, v59, v59
	s_nop 1
	v_mov_b32_dpp v62, v62 quad_perm:[1,0,3,2] row_mask:0xf bank_mask:0xf
	s_waitcnt lgkmcnt(0)
	v_fmac_f32_e32 v62, v59, v59
	s_nop 1
	s_waitcnt lgkmcnt(0)
	v_add_f32_dpp v62, v62, v62 quad_perm:[2,3,0,1] row_mask:0xf bank_mask:0xf
	s_nop 1
	s_waitcnt lgkmcnt(0)
	v_add_f32_dpp v62, v62, v62 row_half_mirror row_mask:0xf bank_mask:0xf
	s_nop 1
	s_waitcnt lgkmcnt(0)
	v_add_f32_dpp v62, v62, v62 row_mirror row_mask:0xf bank_mask:0xf
	v_mov_b32_e32 v63, v62
	s_nop 1
	v_permlane16_swap_b32_e32 v63, v62
	s_waitcnt lgkmcnt(0)
	v_add_f32_e32 v62, v62, v63
	v_mov_b32_e32 v63, v62
	s_nop 1
	v_permlane32_swap_b32_e32 v63, v62
	s_waitcnt lgkmcnt(0)
	v_add_f32_e32 v62, v62, v63
	v_fmamk_f32 v62, v62, 0x3c800000, v164
	v_rsq_f32_e32 v62, v62
	s_nop 0
	v_mul_f32_e32 v59, v59, v62
	v_lshlrev_b32_e32 v62, 16, v157
	v_mul_f32_e32 v62, v231, v62
	v_mul_f32_e32 v63, v62, v172
	s_nop 1
	v_mov_b32_dpp v63, v63 quad_perm:[1,0,3,2] row_mask:0xf bank_mask:0xf
	v_fma_f32 v59, v173, v59, v170
	s_waitcnt lgkmcnt(0)
	v_fmac_f32_e32 v63, v62, v172
	s_nop 1
	s_waitcnt lgkmcnt(0)
	v_add_f32_dpp v62, v63, v63 quad_perm:[2,3,0,1] row_mask:0xf bank_mask:0xf
	s_nop 1
	s_waitcnt lgkmcnt(0)
	v_add_f32_dpp v62, v62, v62 row_half_mirror row_mask:0xf bank_mask:0xf
	s_nop 1
	s_waitcnt lgkmcnt(0)
	v_add_f32_dpp v62, v62, v62 row_mirror row_mask:0xf bank_mask:0xf
	v_mov_b32_e32 v63, v62
	s_nop 1
	v_permlane16_swap_b32_e32 v63, v62
	s_waitcnt lgkmcnt(0)
	v_add_f32_e32 v62, v62, v63
	v_mov_b32_e32 v63, v62
	s_nop 1
	v_permlane32_swap_b32_e32 v63, v62
	s_waitcnt lgkmcnt(0)
	v_add_f32_e32 v62, v62, v63
	v_fmac_f32_e32 v59, v62, v230
	v_mul_f32_e32 v59, v64, v59
	v_cvt_pk_bf16_f32 v58, v59, s0
	global_store_short v[56:57], v58, off offset:512
	v_lshlrev_b32_e32 v56, 16, v155
	v_add_f32_e32 v56, v56, v229
	v_mul_f32_e32 v57, v56, v56
	s_nop 1
	v_mov_b32_dpp v57, v57 quad_perm:[1,0,3,2] row_mask:0xf bank_mask:0xf
	s_waitcnt lgkmcnt(0)
	v_fmac_f32_e32 v57, v56, v56
	s_nop 1
	s_waitcnt lgkmcnt(0)
	v_add_f32_dpp v57, v57, v57 quad_perm:[2,3,0,1] row_mask:0xf bank_mask:0xf
	s_nop 1
	s_waitcnt lgkmcnt(0)
	v_add_f32_dpp v57, v57, v57 row_half_mirror row_mask:0xf bank_mask:0xf
	s_nop 1
	s_waitcnt lgkmcnt(0)
	v_add_f32_dpp v57, v57, v57 row_mirror row_mask:0xf bank_mask:0xf
	v_mov_b32_e32 v58, v57
	s_nop 1
	v_permlane16_swap_b32_e32 v58, v57
	s_waitcnt lgkmcnt(0)
	v_add_f32_e32 v57, v57, v58
	v_mov_b32_e32 v58, v57
	s_nop 1
	v_permlane32_swap_b32_e32 v58, v57
	s_waitcnt lgkmcnt(0)
	v_add_f32_e32 v57, v57, v58
	v_fmamk_f32 v57, v57, 0x3c800000, v165
	v_rsq_f32_e32 v57, v57
	s_nop 0
	v_mul_f32_e32 v56, v56, v57
	v_lshlrev_b32_e32 v57, 16, v156
	v_mul_f32_e32 v58, 0xbfb8aa3b, v57
	v_exp_f32_e32 v58, v58
	v_mul_f32_e32 v56, v176, v56
	v_add_f32_e32 v58, 1.0, v58
	v_rcp_f32_e32 v58, v58
	s_nop 0
	v_mul_f32_e32 v57, v58, v57
	v_mul_f32_e32 v56, v57, v56
	v_lshlrev_b32_e32 v57, 16, v154
	v_add_f32_e32 v57, v57, v228
	s_nop 1
	v_cvt_pk_bf16_f32 v56, v56, s0
	global_store_short v[52:53], v56, off
	s_waitcnt lgkmcnt(0)
	v_add_f32_dpp v58, v57, v57 quad_perm:[1,0,3,2] row_mask:0xf bank_mask:0xf
	s_nop 1
	s_waitcnt lgkmcnt(0)
	v_add_f32_dpp v58, v58, v58 quad_perm:[2,3,0,1] row_mask:0xf bank_mask:0xf
	s_nop 1
	s_waitcnt lgkmcnt(0)
	v_add_f32_dpp v58, v58, v58 row_half_mirror row_mask:0xf bank_mask:0xf
	s_nop 1
	s_waitcnt lgkmcnt(0)
	v_add_f32_dpp v58, v58, v58 row_mirror row_mask:0xf bank_mask:0xf
	v_mov_b32_e32 v59, v58
	s_nop 1
	v_permlane16_swap_b32_e32 v59, v58
	s_waitcnt lgkmcnt(0)
	v_add_f32_e32 v58, v58, v59
	v_mov_b32_e32 v59, v58
	s_nop 1
	v_permlane32_swap_b32_e32 v59, v58
	s_waitcnt lgkmcnt(0)
	v_add_f32_e32 v58, v58, v59
	v_fmac_f32_e32 v57, 0xbc800000, v58
	v_mul_f32_e32 v58, v57, v57
	s_nop 1
	v_mov_b32_dpp v58, v58 quad_perm:[1,0,3,2] row_mask:0xf bank_mask:0xf
	s_waitcnt lgkmcnt(0)
	v_fmac_f32_e32 v58, v57, v57
	s_nop 1
	s_waitcnt lgkmcnt(0)
	v_add_f32_dpp v58, v58, v58 quad_perm:[2,3,0,1] row_mask:0xf bank_mask:0xf
	s_nop 1
	s_waitcnt lgkmcnt(0)
	v_add_f32_dpp v58, v58, v58 row_half_mirror row_mask:0xf bank_mask:0xf
	s_nop 1
	s_waitcnt lgkmcnt(0)
	v_add_f32_dpp v58, v58, v58 row_mirror row_mask:0xf bank_mask:0xf
	v_mov_b32_e32 v59, v58
	s_nop 1
	v_permlane16_swap_b32_e32 v59, v58
	s_waitcnt lgkmcnt(0)
	v_add_f32_e32 v58, v58, v59
	v_mov_b32_e32 v59, v58
	s_nop 1
	v_permlane32_swap_b32_e32 v59, v58
	s_waitcnt lgkmcnt(0)
	v_add_f32_e32 v58, v58, v59
	v_fmamk_f32 v58, v58, 0x3c800000, v164
	v_rsq_f32_e32 v58, v58
	s_nop 0
	v_mul_f32_e32 v57, v57, v58
	v_lshlrev_b32_e32 v58, 16, v153
	v_mul_f32_e32 v58, v227, v58
	v_mul_f32_e32 v59, v58, v172
	s_nop 1
	v_mov_b32_dpp v59, v59 quad_perm:[1,0,3,2] row_mask:0xf bank_mask:0xf
	v_fma_f32 v57, v173, v57, v170
	s_waitcnt lgkmcnt(0)
	v_fmac_f32_e32 v59, v58, v172
	s_nop 1
	s_waitcnt lgkmcnt(0)
	v_add_f32_dpp v58, v59, v59 quad_perm:[2,3,0,1] row_mask:0xf bank_mask:0xf
	s_nop 1
	s_waitcnt lgkmcnt(0)
	v_add_f32_dpp v58, v58, v58 row_half_mirror row_mask:0xf bank_mask:0xf
	s_nop 1
	s_waitcnt lgkmcnt(0)
	v_add_f32_dpp v58, v58, v58 row_mirror row_mask:0xf bank_mask:0xf
	v_mov_b32_e32 v59, v58
	s_nop 1
	v_permlane16_swap_b32_e32 v59, v58
	s_waitcnt lgkmcnt(0)
	v_add_f32_e32 v58, v58, v59
	v_mov_b32_e32 v59, v58
	s_nop 1
	v_permlane32_swap_b32_e32 v59, v58
	s_waitcnt lgkmcnt(0)
	v_add_f32_e32 v58, v58, v59
	v_fmac_f32_e32 v57, v58, v226
	v_mul_f32_e32 v57, v65, v57
	v_cvt_pk_bf16_f32 v56, v57, s0
	global_store_short v[52:53], v56, off offset:512
	v_lshlrev_b32_e32 v52, 16, v151
	v_add_f32_e32 v52, v52, v225
	v_mul_f32_e32 v53, v52, v52
	s_nop 1
	v_mov_b32_dpp v53, v53 quad_perm:[1,0,3,2] row_mask:0xf bank_mask:0xf
	s_waitcnt lgkmcnt(0)
	v_fmac_f32_e32 v53, v52, v52
	s_nop 1
	s_waitcnt lgkmcnt(0)
	v_add_f32_dpp v53, v53, v53 quad_perm:[2,3,0,1] row_mask:0xf bank_mask:0xf
	s_nop 1
	s_waitcnt lgkmcnt(0)
	v_add_f32_dpp v53, v53, v53 row_half_mirror row_mask:0xf bank_mask:0xf
	s_nop 1
	s_waitcnt lgkmcnt(0)
	v_add_f32_dpp v53, v53, v53 row_mirror row_mask:0xf bank_mask:0xf
	v_mov_b32_e32 v56, v53
	s_nop 1
	v_permlane16_swap_b32_e32 v56, v53
	s_waitcnt lgkmcnt(0)
	v_add_f32_e32 v53, v53, v56
	v_mov_b32_e32 v56, v53
	s_nop 1
	v_permlane32_swap_b32_e32 v56, v53
	s_waitcnt lgkmcnt(0)
	v_add_f32_e32 v53, v53, v56
	v_fmamk_f32 v53, v53, 0x3c800000, v165
	v_rsq_f32_e32 v53, v53
	s_nop 0
	v_mul_f32_e32 v52, v52, v53
	v_lshlrev_b32_e32 v53, 16, v152
	v_mul_f32_e32 v56, 0xbfb8aa3b, v53
	v_exp_f32_e32 v56, v56
	v_mul_f32_e32 v52, v176, v52
	v_add_f32_e32 v56, 1.0, v56
	v_rcp_f32_e32 v56, v56
	s_nop 0
	v_mul_f32_e32 v53, v56, v53
	v_mul_f32_e32 v52, v53, v52
	v_lshlrev_b32_e32 v53, 16, v150
	v_add_f32_e32 v53, v53, v224
	s_nop 1
	v_cvt_pk_bf16_f32 v52, v52, s0
	global_store_short v[50:51], v52, off
	s_waitcnt lgkmcnt(0)
	v_add_f32_dpp v56, v53, v53 quad_perm:[1,0,3,2] row_mask:0xf bank_mask:0xf
	s_nop 1
	s_waitcnt lgkmcnt(0)
	v_add_f32_dpp v56, v56, v56 quad_perm:[2,3,0,1] row_mask:0xf bank_mask:0xf
	s_nop 1
	s_waitcnt lgkmcnt(0)
	v_add_f32_dpp v56, v56, v56 row_half_mirror row_mask:0xf bank_mask:0xf
	s_nop 1
	s_waitcnt lgkmcnt(0)
	v_add_f32_dpp v56, v56, v56 row_mirror row_mask:0xf bank_mask:0xf
	v_mov_b32_e32 v57, v56
	s_nop 1
	v_permlane16_swap_b32_e32 v57, v56
	s_waitcnt lgkmcnt(0)
	v_add_f32_e32 v56, v56, v57
	v_mov_b32_e32 v57, v56
	s_nop 1
	v_permlane32_swap_b32_e32 v57, v56
	s_waitcnt lgkmcnt(0)
	v_add_f32_e32 v56, v56, v57
	v_fmac_f32_e32 v53, 0xbc800000, v56
	v_mul_f32_e32 v56, v53, v53
	s_nop 1
	v_mov_b32_dpp v56, v56 quad_perm:[1,0,3,2] row_mask:0xf bank_mask:0xf
	s_waitcnt lgkmcnt(0)
	v_fmac_f32_e32 v56, v53, v53
	s_nop 1
	s_waitcnt lgkmcnt(0)
	v_add_f32_dpp v56, v56, v56 quad_perm:[2,3,0,1] row_mask:0xf bank_mask:0xf
	s_nop 1
	s_waitcnt lgkmcnt(0)
	v_add_f32_dpp v56, v56, v56 row_half_mirror row_mask:0xf bank_mask:0xf
	s_nop 1
	s_waitcnt lgkmcnt(0)
	v_add_f32_dpp v56, v56, v56 row_mirror row_mask:0xf bank_mask:0xf
	v_mov_b32_e32 v57, v56
	s_nop 1
	v_permlane16_swap_b32_e32 v57, v56
	s_waitcnt lgkmcnt(0)
	v_add_f32_e32 v56, v56, v57
	v_mov_b32_e32 v57, v56
	s_nop 1
	v_permlane32_swap_b32_e32 v57, v56
	s_waitcnt lgkmcnt(0)
	v_add_f32_e32 v56, v56, v57
	v_fmamk_f32 v56, v56, 0x3c800000, v164
	v_rsq_f32_e32 v56, v56
	s_nop 0
	v_mul_f32_e32 v53, v53, v56
	v_lshlrev_b32_e32 v56, 16, v149
	v_mul_f32_e32 v56, v191, v56
	v_mul_f32_e32 v57, v56, v172
	s_nop 1
	v_mov_b32_dpp v57, v57 quad_perm:[1,0,3,2] row_mask:0xf bank_mask:0xf
	v_fma_f32 v53, v173, v53, v170
	s_waitcnt lgkmcnt(0)
	v_fmac_f32_e32 v57, v56, v172
	s_nop 1
	s_waitcnt lgkmcnt(0)
	v_add_f32_dpp v56, v57, v57 quad_perm:[2,3,0,1] row_mask:0xf bank_mask:0xf
	s_nop 1
	s_waitcnt lgkmcnt(0)
	v_add_f32_dpp v56, v56, v56 row_half_mirror row_mask:0xf bank_mask:0xf
	s_nop 1
	s_waitcnt lgkmcnt(0)
	v_add_f32_dpp v56, v56, v56 row_mirror row_mask:0xf bank_mask:0xf
	v_mov_b32_e32 v57, v56
	s_nop 1
	v_permlane16_swap_b32_e32 v57, v56
	s_waitcnt lgkmcnt(0)
	v_add_f32_e32 v56, v56, v57
	v_mov_b32_e32 v57, v56
	s_nop 1
	v_permlane32_swap_b32_e32 v57, v56
	s_waitcnt lgkmcnt(0)
	v_add_f32_e32 v56, v56, v57
	v_fmac_f32_e32 v53, v56, v190
	v_mul_f32_e32 v53, v60, v53
	v_cvt_pk_bf16_f32 v52, v53, s0
	global_store_short v[50:51], v52, off offset:512
	v_lshlrev_b32_e32 v50, 16, v147
	v_add_f32_e32 v50, v50, v189
	v_mul_f32_e32 v51, v50, v50
	s_nop 1
	v_mov_b32_dpp v51, v51 quad_perm:[1,0,3,2] row_mask:0xf bank_mask:0xf
	s_waitcnt lgkmcnt(0)
	v_fmac_f32_e32 v51, v50, v50
	s_nop 1
	s_waitcnt lgkmcnt(0)
	v_add_f32_dpp v51, v51, v51 quad_perm:[2,3,0,1] row_mask:0xf bank_mask:0xf
	s_nop 1
	s_waitcnt lgkmcnt(0)
	v_add_f32_dpp v51, v51, v51 row_half_mirror row_mask:0xf bank_mask:0xf
	s_nop 1
	s_waitcnt lgkmcnt(0)
	v_add_f32_dpp v51, v51, v51 row_mirror row_mask:0xf bank_mask:0xf
	v_mov_b32_e32 v52, v51
	s_nop 1
	v_permlane16_swap_b32_e32 v52, v51
	s_waitcnt lgkmcnt(0)
	v_add_f32_e32 v51, v51, v52
	v_mov_b32_e32 v52, v51
	s_nop 1
	v_permlane32_swap_b32_e32 v52, v51
	s_waitcnt lgkmcnt(0)
	v_add_f32_e32 v51, v51, v52
	v_fmamk_f32 v51, v51, 0x3c800000, v165
	v_rsq_f32_e32 v51, v51
	s_nop 0
	v_mul_f32_e32 v50, v50, v51
	v_lshlrev_b32_e32 v51, 16, v148
	v_mul_f32_e32 v52, 0xbfb8aa3b, v51
	v_exp_f32_e32 v52, v52
	v_mul_f32_e32 v50, v176, v50
	v_add_f32_e32 v52, 1.0, v52
	v_rcp_f32_e32 v52, v52
	s_nop 0
	v_mul_f32_e32 v51, v52, v51
	v_mul_f32_e32 v50, v51, v50
	v_lshlrev_b32_e32 v51, 16, v146
	v_add_f32_e32 v51, v51, v188
	s_nop 1
	v_cvt_pk_bf16_f32 v50, v50, s0
	global_store_short v[48:49], v50, off
	s_waitcnt lgkmcnt(0)
	v_add_f32_dpp v52, v51, v51 quad_perm:[1,0,3,2] row_mask:0xf bank_mask:0xf
	s_nop 1
	s_waitcnt lgkmcnt(0)
	v_add_f32_dpp v52, v52, v52 quad_perm:[2,3,0,1] row_mask:0xf bank_mask:0xf
	s_nop 1
	s_waitcnt lgkmcnt(0)
	v_add_f32_dpp v52, v52, v52 row_half_mirror row_mask:0xf bank_mask:0xf
	s_nop 1
	s_waitcnt lgkmcnt(0)
	v_add_f32_dpp v52, v52, v52 row_mirror row_mask:0xf bank_mask:0xf
	v_mov_b32_e32 v53, v52
	s_nop 1
	v_permlane16_swap_b32_e32 v53, v52
	s_waitcnt lgkmcnt(0)
	v_add_f32_e32 v52, v52, v53
	v_mov_b32_e32 v53, v52
	s_nop 1
	v_permlane32_swap_b32_e32 v53, v52
	s_waitcnt lgkmcnt(0)
	v_add_f32_e32 v52, v52, v53
	v_fmac_f32_e32 v51, 0xbc800000, v52
	v_mul_f32_e32 v52, v51, v51
	s_nop 1
	v_mov_b32_dpp v52, v52 quad_perm:[1,0,3,2] row_mask:0xf bank_mask:0xf
	s_waitcnt lgkmcnt(0)
	v_fmac_f32_e32 v52, v51, v51
	s_nop 1
	s_waitcnt lgkmcnt(0)
	v_add_f32_dpp v52, v52, v52 quad_perm:[2,3,0,1] row_mask:0xf bank_mask:0xf
	s_nop 1
	s_waitcnt lgkmcnt(0)
	v_add_f32_dpp v52, v52, v52 row_half_mirror row_mask:0xf bank_mask:0xf
	s_nop 1
	s_waitcnt lgkmcnt(0)
	v_add_f32_dpp v52, v52, v52 row_mirror row_mask:0xf bank_mask:0xf
	v_mov_b32_e32 v53, v52
	s_nop 1
	v_permlane16_swap_b32_e32 v53, v52
	s_waitcnt lgkmcnt(0)
	v_add_f32_e32 v52, v52, v53
	v_mov_b32_e32 v53, v52
	s_nop 1
	v_permlane32_swap_b32_e32 v53, v52
	s_waitcnt lgkmcnt(0)
	v_add_f32_e32 v52, v52, v53
	v_fmamk_f32 v52, v52, 0x3c800000, v164
	v_rsq_f32_e32 v52, v52
	s_nop 0
	v_mul_f32_e32 v51, v51, v52
	v_lshlrev_b32_e32 v52, 16, v145
	v_mul_f32_e32 v52, v187, v52
	v_mul_f32_e32 v53, v52, v172
	s_nop 1
	v_mov_b32_dpp v53, v53 quad_perm:[1,0,3,2] row_mask:0xf bank_mask:0xf
	v_fma_f32 v51, v173, v51, v170
	s_waitcnt lgkmcnt(0)
	v_fmac_f32_e32 v53, v52, v172
	s_nop 1
	s_waitcnt lgkmcnt(0)
	v_add_f32_dpp v52, v53, v53 quad_perm:[2,3,0,1] row_mask:0xf bank_mask:0xf
	s_nop 1
	s_waitcnt lgkmcnt(0)
	v_add_f32_dpp v52, v52, v52 row_half_mirror row_mask:0xf bank_mask:0xf
	s_nop 1
	s_waitcnt lgkmcnt(0)
	v_add_f32_dpp v52, v52, v52 row_mirror row_mask:0xf bank_mask:0xf
	v_mov_b32_e32 v53, v52
	s_nop 1
	v_permlane16_swap_b32_e32 v53, v52
	s_waitcnt lgkmcnt(0)
	v_add_f32_e32 v52, v52, v53
	v_mov_b32_e32 v53, v52
	s_nop 1
	v_permlane32_swap_b32_e32 v53, v52
	s_waitcnt lgkmcnt(0)
	v_add_f32_e32 v52, v52, v53
	v_fmac_f32_e32 v51, v52, v186
	v_mul_f32_e32 v51, v61, v51
	v_cvt_pk_bf16_f32 v50, v51, s0
	global_store_short v[48:49], v50, off offset:512
	v_lshlrev_b32_e32 v48, 16, v143
	v_add_f32_e32 v48, v48, v185
	v_mul_f32_e32 v49, v48, v48
	s_nop 1
	v_mov_b32_dpp v49, v49 quad_perm:[1,0,3,2] row_mask:0xf bank_mask:0xf
	s_waitcnt lgkmcnt(0)
	v_fmac_f32_e32 v49, v48, v48
	s_nop 1
	s_waitcnt lgkmcnt(0)
	v_add_f32_dpp v49, v49, v49 quad_perm:[2,3,0,1] row_mask:0xf bank_mask:0xf
	s_nop 1
	s_waitcnt lgkmcnt(0)
	v_add_f32_dpp v49, v49, v49 row_half_mirror row_mask:0xf bank_mask:0xf
	s_nop 1
	s_waitcnt lgkmcnt(0)
	v_add_f32_dpp v49, v49, v49 row_mirror row_mask:0xf bank_mask:0xf
	v_mov_b32_e32 v50, v49
	s_nop 1
	v_permlane16_swap_b32_e32 v50, v49
	s_waitcnt lgkmcnt(0)
	v_add_f32_e32 v49, v49, v50
	v_mov_b32_e32 v50, v49
	s_nop 1
	v_permlane32_swap_b32_e32 v50, v49
	s_waitcnt lgkmcnt(0)
	v_add_f32_e32 v49, v49, v50
	v_fmamk_f32 v49, v49, 0x3c800000, v165
	v_rsq_f32_e32 v49, v49
	s_nop 0
	v_mul_f32_e32 v48, v48, v49
	v_lshlrev_b32_e32 v49, 16, v144
	v_mul_f32_e32 v50, 0xbfb8aa3b, v49
	v_exp_f32_e32 v50, v50
	v_mul_f32_e32 v48, v176, v48
	v_add_f32_e32 v50, 1.0, v50
	v_rcp_f32_e32 v50, v50
	s_nop 0
	v_mul_f32_e32 v49, v50, v49
	v_mul_f32_e32 v48, v49, v48
	v_lshlrev_b32_e32 v49, 16, v142
	v_add_f32_e32 v49, v49, v182
	s_nop 1
	v_cvt_pk_bf16_f32 v48, v48, s0
	global_store_short v[46:47], v48, off
	s_waitcnt lgkmcnt(0)
	v_add_f32_dpp v50, v49, v49 quad_perm:[1,0,3,2] row_mask:0xf bank_mask:0xf
	s_nop 1
	s_waitcnt lgkmcnt(0)
	v_add_f32_dpp v50, v50, v50 quad_perm:[2,3,0,1] row_mask:0xf bank_mask:0xf
	s_nop 1
	s_waitcnt lgkmcnt(0)
	v_add_f32_dpp v50, v50, v50 row_half_mirror row_mask:0xf bank_mask:0xf
	s_nop 1
	s_waitcnt lgkmcnt(0)
	v_add_f32_dpp v50, v50, v50 row_mirror row_mask:0xf bank_mask:0xf
	v_mov_b32_e32 v51, v50
	s_nop 1
	v_permlane16_swap_b32_e32 v51, v50
	s_waitcnt lgkmcnt(0)
	v_add_f32_e32 v50, v50, v51
	v_mov_b32_e32 v51, v50
	s_nop 1
	v_permlane32_swap_b32_e32 v51, v50
	s_waitcnt lgkmcnt(0)
	v_add_f32_e32 v50, v50, v51
	v_fmac_f32_e32 v49, 0xbc800000, v50
	v_mul_f32_e32 v50, v49, v49
	s_nop 1
	v_mov_b32_dpp v50, v50 quad_perm:[1,0,3,2] row_mask:0xf bank_mask:0xf
	s_waitcnt lgkmcnt(0)
	v_fmac_f32_e32 v50, v49, v49
	s_nop 1
	s_waitcnt lgkmcnt(0)
	v_add_f32_dpp v50, v50, v50 quad_perm:[2,3,0,1] row_mask:0xf bank_mask:0xf
	s_nop 1
	s_waitcnt lgkmcnt(0)
	v_add_f32_dpp v50, v50, v50 row_half_mirror row_mask:0xf bank_mask:0xf
	s_nop 1
	s_waitcnt lgkmcnt(0)
	v_add_f32_dpp v50, v50, v50 row_mirror row_mask:0xf bank_mask:0xf
	v_mov_b32_e32 v51, v50
	s_nop 1
	v_permlane16_swap_b32_e32 v51, v50
	s_waitcnt lgkmcnt(0)
	v_add_f32_e32 v50, v50, v51
	v_mov_b32_e32 v51, v50
	s_nop 1
	v_permlane32_swap_b32_e32 v51, v50
	s_waitcnt lgkmcnt(0)
	v_add_f32_e32 v50, v50, v51
	v_fmamk_f32 v50, v50, 0x3c800000, v164
	v_rsq_f32_e32 v50, v50
	s_nop 0
	v_mul_f32_e32 v49, v49, v50
	v_lshlrev_b32_e32 v50, 16, v141
	v_mul_f32_e32 v50, v180, v50
	v_mul_f32_e32 v51, v50, v172
	s_nop 1
	v_mov_b32_dpp v51, v51 quad_perm:[1,0,3,2] row_mask:0xf bank_mask:0xf
	v_fma_f32 v49, v173, v49, v170
	s_waitcnt lgkmcnt(0)
	v_fmac_f32_e32 v51, v50, v172
	s_nop 1
	s_waitcnt lgkmcnt(0)
	v_add_f32_dpp v50, v51, v51 quad_perm:[2,3,0,1] row_mask:0xf bank_mask:0xf
	s_nop 1
	s_waitcnt lgkmcnt(0)
	v_add_f32_dpp v50, v50, v50 row_half_mirror row_mask:0xf bank_mask:0xf
	s_nop 1
	s_waitcnt lgkmcnt(0)
	v_add_f32_dpp v50, v50, v50 row_mirror row_mask:0xf bank_mask:0xf
	v_mov_b32_e32 v51, v50
	s_nop 1
	v_permlane16_swap_b32_e32 v51, v50
	s_waitcnt lgkmcnt(0)
	v_add_f32_e32 v50, v50, v51
	v_mov_b32_e32 v51, v50
	s_nop 1
	v_permlane32_swap_b32_e32 v51, v50
	s_waitcnt lgkmcnt(0)
	v_add_f32_e32 v50, v50, v51
	v_fmac_f32_e32 v49, v50, v175
	v_mul_f32_e32 v49, v54, v49
	v_cvt_pk_bf16_f32 v48, v49, s0
	global_store_short v[46:47], v48, off offset:512
	v_lshlrev_b32_e32 v46, 16, v139
	v_add_f32_e32 v46, v46, v174
	v_mul_f32_e32 v47, v46, v46
	s_nop 1
	v_mov_b32_dpp v47, v47 quad_perm:[1,0,3,2] row_mask:0xf bank_mask:0xf
	s_waitcnt lgkmcnt(0)
	v_fmac_f32_e32 v47, v46, v46
	s_nop 1
	s_waitcnt lgkmcnt(0)
	v_add_f32_dpp v47, v47, v47 quad_perm:[2,3,0,1] row_mask:0xf bank_mask:0xf
	s_nop 1
	s_waitcnt lgkmcnt(0)
	v_add_f32_dpp v47, v47, v47 row_half_mirror row_mask:0xf bank_mask:0xf
	s_nop 1
	s_waitcnt lgkmcnt(0)
	v_add_f32_dpp v47, v47, v47 row_mirror row_mask:0xf bank_mask:0xf
	v_mov_b32_e32 v48, v47
	s_nop 1
	v_permlane16_swap_b32_e32 v48, v47
	s_waitcnt lgkmcnt(0)
	v_add_f32_e32 v47, v47, v48
	v_mov_b32_e32 v48, v47
	s_nop 1
	v_permlane32_swap_b32_e32 v48, v47
	s_waitcnt lgkmcnt(0)
	v_add_f32_e32 v47, v47, v48
	v_fmamk_f32 v47, v47, 0x3c800000, v165
	v_rsq_f32_e32 v47, v47
	s_nop 0
	v_mul_f32_e32 v46, v46, v47
	v_lshlrev_b32_e32 v47, 16, v140
	v_mul_f32_e32 v48, 0xbfb8aa3b, v47
	v_exp_f32_e32 v48, v48
	v_mul_f32_e32 v46, v176, v46
	v_add_f32_e32 v48, 1.0, v48
	v_rcp_f32_e32 v48, v48
	s_nop 0
	v_mul_f32_e32 v47, v48, v47
	v_mul_f32_e32 v46, v47, v46
	v_lshlrev_b32_e32 v47, 16, v138
	v_add_f32_e32 v47, v47, v171
	s_nop 1
	v_cvt_pk_bf16_f32 v46, v46, s0
	global_store_short v[44:45], v46, off
	s_waitcnt lgkmcnt(0)
	v_add_f32_dpp v48, v47, v47 quad_perm:[1,0,3,2] row_mask:0xf bank_mask:0xf
	s_nop 1
	s_waitcnt lgkmcnt(0)
	v_add_f32_dpp v48, v48, v48 quad_perm:[2,3,0,1] row_mask:0xf bank_mask:0xf
	s_nop 1
	s_waitcnt lgkmcnt(0)
	v_add_f32_dpp v48, v48, v48 row_half_mirror row_mask:0xf bank_mask:0xf
	s_nop 1
	s_waitcnt lgkmcnt(0)
	v_add_f32_dpp v48, v48, v48 row_mirror row_mask:0xf bank_mask:0xf
	v_mov_b32_e32 v49, v48
	s_nop 1
	v_permlane16_swap_b32_e32 v49, v48
	s_waitcnt lgkmcnt(0)
	v_add_f32_e32 v48, v48, v49
	v_mov_b32_e32 v49, v48
	s_nop 1
	v_permlane32_swap_b32_e32 v49, v48
	s_waitcnt lgkmcnt(0)
	v_add_f32_e32 v48, v48, v49
	v_fmac_f32_e32 v47, 0xbc800000, v48
	v_mul_f32_e32 v48, v47, v47
	s_nop 1
	v_mov_b32_dpp v48, v48 quad_perm:[1,0,3,2] row_mask:0xf bank_mask:0xf
	s_waitcnt lgkmcnt(0)
	v_fmac_f32_e32 v48, v47, v47
	s_nop 1
	s_waitcnt lgkmcnt(0)
	v_add_f32_dpp v48, v48, v48 quad_perm:[2,3,0,1] row_mask:0xf bank_mask:0xf
	s_nop 1
	s_waitcnt lgkmcnt(0)
	v_add_f32_dpp v48, v48, v48 row_half_mirror row_mask:0xf bank_mask:0xf
	s_nop 1
	s_waitcnt lgkmcnt(0)
	v_add_f32_dpp v48, v48, v48 row_mirror row_mask:0xf bank_mask:0xf
	v_mov_b32_e32 v49, v48
	s_nop 1
	v_permlane16_swap_b32_e32 v49, v48
	s_waitcnt lgkmcnt(0)
	v_add_f32_e32 v48, v48, v49
	v_mov_b32_e32 v49, v48
	s_nop 1
	v_permlane32_swap_b32_e32 v49, v48
	s_waitcnt lgkmcnt(0)
	v_add_f32_e32 v48, v48, v49
	v_fmamk_f32 v48, v48, 0x3c800000, v164
	v_rsq_f32_e32 v48, v48
	s_nop 0
	v_mul_f32_e32 v47, v47, v48
	v_fmac_f32_e32 v170, v173, v47
	v_lshlrev_b32_e32 v47, 16, v137
	v_mul_f32_e32 v47, v169, v47
	v_mul_f32_e32 v48, v47, v172
	s_nop 1
	v_mov_b32_dpp v48, v48 quad_perm:[1,0,3,2] row_mask:0xf bank_mask:0xf
	s_waitcnt lgkmcnt(0)
	v_fmac_f32_e32 v48, v47, v172
	s_nop 1
	s_waitcnt lgkmcnt(0)
	v_add_f32_dpp v47, v48, v48 quad_perm:[2,3,0,1] row_mask:0xf bank_mask:0xf
	s_nop 1
	s_waitcnt lgkmcnt(0)
	v_add_f32_dpp v47, v47, v47 row_half_mirror row_mask:0xf bank_mask:0xf
	s_nop 1
	s_waitcnt lgkmcnt(0)
	v_add_f32_dpp v47, v47, v47 row_mirror row_mask:0xf bank_mask:0xf
	v_mov_b32_e32 v48, v47
	s_nop 1
	v_permlane16_swap_b32_e32 v48, v47
	s_waitcnt lgkmcnt(0)
	v_add_f32_e32 v47, v47, v48
	v_mov_b32_e32 v48, v47
	s_nop 1
	v_permlane32_swap_b32_e32 v48, v47
	s_waitcnt lgkmcnt(0)
	v_add_f32_e32 v47, v47, v48
	v_fmac_f32_e32 v170, v47, v163
	v_mul_f32_e32 v47, v55, v170
	v_cvt_pk_bf16_f32 v46, v47, s0
	global_store_short v[44:45], v46, off offset:512
	global_load_dword v45, v[30:31], off
	s_nop 0
	global_load_dword v44, v[32:33], off
	v_lshlrev_b32_e32 v46, 16, v135
	v_add_f32_e32 v46, v46, v71
	v_lshlrev_b32_e32 v47, 16, v136
	s_waitcnt vmcnt(1)
	v_fmac_f32_e32 v46, v45, v47
	v_mul_f32_e32 v47, 0xbfb8aa3b, v70
	v_exp_f32_e32 v47, v47
	s_nop 0
	v_add_f32_e32 v47, 1.0, v47
	v_rcp_f32_e32 v47, v47
	s_nop 0
	v_mul_f32_e32 v47, v47, v70
	v_mul_f32_e32 v46, v47, v46
	v_mul_f32_e32 v47, v46, v46
	s_nop 1
	v_mov_b32_dpp v47, v47 quad_perm:[1,0,3,2] row_mask:0xf bank_mask:0xf
	s_waitcnt lgkmcnt(0)
	v_fmac_f32_e32 v47, v46, v46
	s_nop 1
	s_waitcnt lgkmcnt(0)
	v_add_f32_dpp v47, v47, v47 quad_perm:[2,3,0,1] row_mask:0xf bank_mask:0xf
	s_nop 1
	s_waitcnt lgkmcnt(0)
	v_add_f32_dpp v47, v47, v47 row_half_mirror row_mask:0xf bank_mask:0xf
	s_nop 1
	s_waitcnt lgkmcnt(0)
	v_add_f32_dpp v47, v47, v47 row_mirror row_mask:0xf bank_mask:0xf
	v_mov_b32_e32 v48, v47
	s_nop 1
	v_permlane16_swap_b32_e32 v48, v47
	s_waitcnt lgkmcnt(0)
	v_add_f32_e32 v47, v47, v48
	v_mov_b32_e32 v48, v47
	s_nop 1
	v_permlane32_swap_b32_e32 v48, v47
	s_and_saveexec_b64 s[0:1], vcc
	s_cbranch_execz .LBB0_1237
	s_waitcnt lgkmcnt(0)
	v_add_f32_e32 v47, v47, v48
	v_mov_b32_e32 v48, s11
	ds_write_b32 v48, v47 offset:4096
